# v59 + grid barrier: every acquire invalidate (leader, waiters, local barrier) issued at arrival so it completes under the wait
# speedup vs baseline: 1.0080x; 1.0080x over previous
.LBB0_1033:
	s_andn2_saveexec_b64 s[14:15], s[14:15]
	s_cbranch_execz .LBB0_2078
	s_mov_b64 s[14:15], exec
	buffer_wbl2 sc1
	buffer_inv sc1
	s_waitcnt lgkmcnt(0)
	s_waitcnt vmcnt(0)
	v_mbcnt_lo_u32_b32 v0, s14, 0
	v_mbcnt_hi_u32_b32 v0, s15, v0
	v_cmp_eq_u32_e32 vcc, 0, v0
	s_and_saveexec_b64 s[16:17], vcc
	s_cbranch_execz .LBB0_1036
	s_bcnt1_i32_b64 s14, s[14:15]
	v_mov_b32_e32 v3, s14
	v_readlane_b32 s14, v251, 37
	v_readlane_b32 s15, v251, 38
	s_nop 4
	global_atomic_add v3, v1, v3, s[14:15] sc0

.LBB0_2077:
	s_or_b64 exec, exec, s[14:15]
	v_readlane_b32 s14, v250, 33
	v_readlane_b32 s15, v250, 34
	s_waitcnt vmcnt(0)
	s_nop 2
	global_atomic_add v1, v225, s[14:15]
	s_waitcnt vmcnt(0)
